# v108 + first K-loop iteration peeled (zero addend, no accumulator zeroing block) also in the two k5 GEMM copies and the k6 copy
# baseline (speedup 1.0000x reference)
.LBB0_910:
	s_add_u32 s52, s52, 0x80080
	s_addc_u32 s53, s53, 0
	s_add_u32 s8, s36, 0x100
	v_mov_b32_e32 v2, 0
	s_addc_u32 s9, s37, 0
	s_mov_b32 s71, -2
	s_add_u32 s10, s52, 0xfff80080
	s_addc_u32 s11, s53, -1
	s_add_i32 s12, 0, 0x10000
	s_cmp_eq_u32 s71, 28
	s_cselect_b32 s55, s47, s11
	s_cselect_b32 s54, s46, s10
	s_cselect_b32 s37, s49, s9
	s_cselect_b32 s36, s48, s8
	s_add_i32 s13, 0, 0x14000
	v_add_u32_e32 v158, s12, v147
	v_add_u32_e32 v174, s13, v147
	ds_read_b128 v[142:145], v158
	ds_read_b128 v[150:153], v158 offset:1024
	ds_read_b128 v[154:157], v158 offset:2048
	ds_read_b128 v[158:161], v158 offset:3072
	ds_read_b128 v[162:165], v174
	ds_read_b128 v[166:169], v174 offset:1024
	ds_read_b128 v[170:173], v174 offset:2048
	ds_read_b128 v[174:177], v174 offset:3072
	v_lshl_add_u64 v[202:203], s[52:53], 0, v[138:139]
	s_add_i32 m0, s59, 0xc000
	ds_read_b128 v[178:181], v149
	ds_read_b128 v[182:185], v149 offset:1024
	ds_read_b128 v[186:189], v149 offset:2048
	ds_read_b128 v[190:193], v149 offset:3072
	ds_read_b128 v[194:197], v149 offset:4096
	ds_read_b128 v[198:201], v149 offset:5120
	ds_read_b128 v[208:211], v149 offset:6144
	ds_read_b128 v[212:215], v149 offset:7168
	global_load_lds_dwordx4 v[202:203], off
	v_lshl_add_u64 v[202:203], s[52:53], 0, v[140:141]
	s_add_i32 m0, s59, 0xe000
	s_nop 0
	global_load_lds_dwordx4 v[202:203], off
	s_waitcnt vmcnt(8)
	s_waitcnt lgkmcnt(0)
	s_barrier
	s_setprio 1
	s_waitcnt lgkmcnt(0)
	v_mfma_f32_16x16x32_bf16 v[128:131], v[142:145], v[178:181], 0
	v_mfma_f32_16x16x32_bf16 v[124:127], v[154:157], v[178:181], 0
	v_mfma_f32_16x16x32_bf16 v[116:119], v[142:145], v[186:189], 0
	v_mfma_f32_16x16x32_bf16 v[108:111], v[154:157], v[186:189], 0
	v_mfma_f32_16x16x32_bf16 v[100:103], v[142:145], v[194:197], 0
	v_mfma_f32_16x16x32_bf16 v[92:95], v[154:157], v[194:197], 0
	v_mfma_f32_16x16x32_bf16 v[84:87], v[142:145], v[208:211], 0
	v_mfma_f32_16x16x32_bf16 v[76:79], v[154:157], v[208:211], 0
	v_mfma_f32_16x16x32_bf16 v[128:131], v[150:153], v[182:185], v[128:131]
	v_mfma_f32_16x16x32_bf16 v[124:127], v[158:161], v[182:185], v[124:127]
	v_mfma_f32_16x16x32_bf16 v[116:119], v[150:153], v[190:193], v[116:119]
	v_mfma_f32_16x16x32_bf16 v[108:111], v[158:161], v[190:193], v[108:111]
	v_mfma_f32_16x16x32_bf16 v[100:103], v[150:153], v[198:201], v[100:103]
	v_mfma_f32_16x16x32_bf16 v[92:95], v[158:161], v[198:201], v[92:95]
	v_mfma_f32_16x16x32_bf16 v[84:87], v[150:153], v[212:215], v[84:87]
	v_mfma_f32_16x16x32_bf16 v[76:79], v[158:161], v[212:215], v[76:79]
	s_setprio 0
	s_setprio 1
	v_mfma_f32_16x16x32_bf16 v[120:123], v[162:165], v[178:181], 0
	v_mfma_f32_16x16x32_bf16 v[112:115], v[170:173], v[178:181], 0
	v_mfma_f32_16x16x32_bf16 v[104:107], v[162:165], v[186:189], 0
	v_mfma_f32_16x16x32_bf16 v[96:99], v[170:173], v[186:189], 0
	v_mfma_f32_16x16x32_bf16 v[88:91], v[162:165], v[194:197], 0
	v_mfma_f32_16x16x32_bf16 v[80:83], v[170:173], v[194:197], 0
	v_mfma_f32_16x16x32_bf16 v[72:75], v[162:165], v[208:211], 0
	v_mfma_f32_16x16x32_bf16 v[68:71], v[170:173], v[208:211], 0
	v_mfma_f32_16x16x32_bf16 v[120:123], v[166:169], v[182:185], v[120:123]
	v_mfma_f32_16x16x32_bf16 v[112:115], v[174:177], v[182:185], v[112:115]
	v_mfma_f32_16x16x32_bf16 v[104:107], v[166:169], v[190:193], v[104:107]
	v_mfma_f32_16x16x32_bf16 v[96:99], v[174:177], v[190:193], v[96:99]
	v_mfma_f32_16x16x32_bf16 v[88:91], v[166:169], v[198:201], v[88:91]
	v_mfma_f32_16x16x32_bf16 v[80:83], v[174:177], v[198:201], v[80:83]
	v_mfma_f32_16x16x32_bf16 v[72:75], v[166:169], v[212:215], v[72:75]
	v_mfma_f32_16x16x32_bf16 v[68:71], v[174:177], v[212:215], v[68:71]
	s_setprio 0
	s_barrier
	s_add_i32 s10, s12, s58
	v_lshl_add_u64 v[202:203], s[36:37], 0, v[66:67]
	s_mov_b32 m0, s10
	ds_read_b128 v[178:181], v149 offset:16384
	ds_read_b128 v[182:185], v149 offset:17408
	ds_read_b128 v[186:189], v149 offset:18432
	ds_read_b128 v[190:193], v149 offset:19456
	ds_read_b128 v[194:197], v149 offset:20480
	ds_read_b128 v[198:201], v149 offset:21504
	ds_read_b128 v[208:211], v149 offset:22528
	ds_read_b128 v[212:215], v149 offset:23552
	global_load_lds_dwordx4 v[202:203], off
	s_add_i32 m0, s10, 0x2000
	s_add_u32 s10, s36, 0x80000
	v_lshl_add_u64 v[216:217], s[36:37], 0, v[136:137]
	s_addc_u32 s11, s37, 0
	s_add_i32 s12, s13, s58
	global_load_lds_dwordx4 v[216:217], off
	v_lshl_add_u64 v[218:219], s[10:11], 0, v[66:67]
	s_mov_b32 m0, s12
	v_lshl_add_u64 v[220:221], s[54:55], 0, v[134:135]
	global_load_lds_dwordx4 v[218:219], off
	v_lshl_add_u64 v[218:219], s[10:11], 0, v[136:137]
	s_add_i32 m0, s12, 0x2000
	s_nop 0
	global_load_lds_dwordx4 v[218:219], off
	v_lshl_add_u64 v[218:219], s[54:55], 0, v[132:133]
	s_mov_b32 m0, s59
	s_nop 0
	global_load_lds_dwordx4 v[218:219], off
	s_mov_b32 m0, s64
	s_nop 0
	global_load_lds_dwordx4 v[220:221], off
	s_waitcnt vmcnt(8)
	s_waitcnt lgkmcnt(0)
	s_barrier
	s_setprio 1
	s_waitcnt lgkmcnt(0)
	v_mfma_f32_16x16x32_bf16 v[62:65], v[142:145], v[178:181], 0
	v_mfma_f32_16x16x32_bf16 v[58:61], v[154:157], v[178:181], 0
	v_mfma_f32_16x16x32_bf16 v[50:53], v[142:145], v[186:189], 0
	v_mfma_f32_16x16x32_bf16 v[42:45], v[154:157], v[186:189], 0
	v_mfma_f32_16x16x32_bf16 v[34:37], v[142:145], v[194:197], 0
	v_mfma_f32_16x16x32_bf16 v[26:29], v[154:157], v[194:197], 0
	v_mfma_f32_16x16x32_bf16 v[18:21], v[142:145], v[208:211], 0
	v_mfma_f32_16x16x32_bf16 v[10:13], v[154:157], v[208:211], 0
	v_mfma_f32_16x16x32_bf16 v[62:65], v[150:153], v[182:185], v[62:65]
	v_mfma_f32_16x16x32_bf16 v[58:61], v[158:161], v[182:185], v[58:61]
	v_mfma_f32_16x16x32_bf16 v[50:53], v[150:153], v[190:193], v[50:53]
	v_mfma_f32_16x16x32_bf16 v[42:45], v[158:161], v[190:193], v[42:45]
	v_mfma_f32_16x16x32_bf16 v[34:37], v[150:153], v[198:201], v[34:37]
	v_mfma_f32_16x16x32_bf16 v[26:29], v[158:161], v[198:201], v[26:29]
	v_mfma_f32_16x16x32_bf16 v[18:21], v[150:153], v[212:215], v[18:21]
	v_mfma_f32_16x16x32_bf16 v[10:13], v[158:161], v[212:215], v[10:13]
	s_setprio 0
	s_setprio 1
	v_mfma_f32_16x16x32_bf16 v[54:57], v[162:165], v[178:181], 0
	v_mfma_f32_16x16x32_bf16 v[46:49], v[170:173], v[178:181], 0
	v_mfma_f32_16x16x32_bf16 v[38:41], v[162:165], v[186:189], 0
	v_mfma_f32_16x16x32_bf16 v[30:33], v[170:173], v[186:189], 0
	v_mfma_f32_16x16x32_bf16 v[22:25], v[162:165], v[194:197], 0
	v_mfma_f32_16x16x32_bf16 v[14:17], v[170:173], v[194:197], 0
	v_mfma_f32_16x16x32_bf16 v[6:9], v[162:165], v[208:211], 0
	v_mfma_f32_16x16x32_bf16 v[2:5], v[170:173], v[208:211], 0
	v_mfma_f32_16x16x32_bf16 v[54:57], v[166:169], v[182:185], v[54:57]
	v_mfma_f32_16x16x32_bf16 v[46:49], v[174:177], v[182:185], v[46:49]
	v_mfma_f32_16x16x32_bf16 v[38:41], v[166:169], v[190:193], v[38:41]
	v_mfma_f32_16x16x32_bf16 v[30:33], v[174:177], v[190:193], v[30:33]
	v_mfma_f32_16x16x32_bf16 v[22:25], v[166:169], v[198:201], v[22:25]
	v_mfma_f32_16x16x32_bf16 v[14:17], v[174:177], v[198:201], v[14:17]
	v_mfma_f32_16x16x32_bf16 v[6:9], v[166:169], v[212:215], v[6:9]
	v_mfma_f32_16x16x32_bf16 v[2:5], v[174:177], v[212:215], v[2:5]
	s_setprio 0
	s_barrier
	s_add_i32 s12, 0, 0x18000
	s_add_i32 s13, 0, 0x1c000
	v_add_u32_e32 v158, s12, v147
	v_add_u32_e32 v174, s13, v147
	ds_read_b128 v[142:145], v158
	ds_read_b128 v[150:153], v158 offset:1024
	ds_read_b128 v[154:157], v158 offset:2048
	ds_read_b128 v[158:161], v158 offset:3072
	ds_read_b128 v[162:165], v174
	ds_read_b128 v[166:169], v174 offset:1024
	ds_read_b128 v[170:173], v174 offset:2048
	ds_read_b128 v[174:177], v174 offset:3072
	s_add_u32 s10, s54, 0x80000
	s_addc_u32 s11, s55, 0
	s_mov_b32 m0, s65
	v_lshl_add_u64 v[222:223], s[10:11], 0, v[132:133]
	ds_read_b128 v[178:181], v149 offset:32768
	ds_read_b128 v[182:185], v149 offset:33792
	ds_read_b128 v[186:189], v149 offset:34816
	ds_read_b128 v[190:193], v149 offset:35840
	ds_read_b128 v[194:197], v149 offset:36864
	ds_read_b128 v[198:201], v149 offset:37888
	ds_read_b128 v[208:211], v149 offset:38912
	ds_read_b128 v[212:215], v149 offset:39936
	global_load_lds_dwordx4 v[222:223], off
	v_lshl_add_u64 v[222:223], s[10:11], 0, v[134:135]
	s_mov_b32 m0, s66
	s_nop 0
	global_load_lds_dwordx4 v[222:223], off
	s_waitcnt vmcnt(8)
	s_waitcnt lgkmcnt(0)
	s_barrier
	s_setprio 1
	s_waitcnt lgkmcnt(0)
	v_mfma_f32_16x16x32_bf16 v[128:131], v[142:145], v[178:181], v[128:131]
	v_mfma_f32_16x16x32_bf16 v[124:127], v[154:157], v[178:181], v[124:127]
	v_mfma_f32_16x16x32_bf16 v[116:119], v[142:145], v[186:189], v[116:119]
	v_mfma_f32_16x16x32_bf16 v[108:111], v[154:157], v[186:189], v[108:111]
	v_mfma_f32_16x16x32_bf16 v[100:103], v[142:145], v[194:197], v[100:103]
	v_mfma_f32_16x16x32_bf16 v[92:95], v[154:157], v[194:197], v[92:95]
	v_mfma_f32_16x16x32_bf16 v[84:87], v[142:145], v[208:211], v[84:87]
	v_mfma_f32_16x16x32_bf16 v[76:79], v[154:157], v[208:211], v[76:79]
	v_mfma_f32_16x16x32_bf16 v[128:131], v[150:153], v[182:185], v[128:131]
	v_mfma_f32_16x16x32_bf16 v[124:127], v[158:161], v[182:185], v[124:127]
	v_mfma_f32_16x16x32_bf16 v[116:119], v[150:153], v[190:193], v[116:119]
	v_mfma_f32_16x16x32_bf16 v[108:111], v[158:161], v[190:193], v[108:111]
	v_mfma_f32_16x16x32_bf16 v[100:103], v[150:153], v[198:201], v[100:103]
	v_mfma_f32_16x16x32_bf16 v[92:95], v[158:161], v[198:201], v[92:95]
	v_mfma_f32_16x16x32_bf16 v[84:87], v[150:153], v[212:215], v[84:87]
	v_mfma_f32_16x16x32_bf16 v[76:79], v[158:161], v[212:215], v[76:79]
	s_setprio 0
	s_setprio 1
	v_mfma_f32_16x16x32_bf16 v[120:123], v[162:165], v[178:181], v[120:123]
	v_mfma_f32_16x16x32_bf16 v[112:115], v[170:173], v[178:181], v[112:115]
	v_mfma_f32_16x16x32_bf16 v[104:107], v[162:165], v[186:189], v[104:107]
	v_mfma_f32_16x16x32_bf16 v[96:99], v[170:173], v[186:189], v[96:99]
	v_mfma_f32_16x16x32_bf16 v[88:91], v[162:165], v[194:197], v[88:91]
	v_mfma_f32_16x16x32_bf16 v[80:83], v[170:173], v[194:197], v[80:83]
	v_mfma_f32_16x16x32_bf16 v[72:75], v[162:165], v[208:211], v[72:75]
	v_mfma_f32_16x16x32_bf16 v[68:71], v[170:173], v[208:211], v[68:71]
	v_mfma_f32_16x16x32_bf16 v[120:123], v[166:169], v[182:185], v[120:123]
	v_mfma_f32_16x16x32_bf16 v[112:115], v[174:177], v[182:185], v[112:115]
	v_mfma_f32_16x16x32_bf16 v[104:107], v[166:169], v[190:193], v[104:107]
	v_mfma_f32_16x16x32_bf16 v[96:99], v[174:177], v[190:193], v[96:99]
	v_mfma_f32_16x16x32_bf16 v[88:91], v[166:169], v[198:201], v[88:91]
	v_mfma_f32_16x16x32_bf16 v[80:83], v[174:177], v[198:201], v[80:83]
	v_mfma_f32_16x16x32_bf16 v[72:75], v[166:169], v[212:215], v[72:75]
	v_mfma_f32_16x16x32_bf16 v[68:71], v[174:177], v[212:215], v[68:71]
	s_setprio 0
	s_barrier
	s_add_i32 s10, s12, s58
	v_lshl_add_u64 v[202:203], v[202:203], 0, s[60:61]
	s_mov_b32 m0, s10
	ds_read_b128 v[178:181], v149 offset:49152
	ds_read_b128 v[182:185], v149 offset:50176
	ds_read_b128 v[186:189], v149 offset:51200
	ds_read_b128 v[190:193], v149 offset:52224
	ds_read_b128 v[194:197], v149 offset:53248
	ds_read_b128 v[198:201], v149 offset:54272
	ds_read_b128 v[208:211], v149 offset:55296
	ds_read_b128 v[212:215], v149 offset:56320
	global_load_lds_dwordx4 v[202:203], off
	s_add_i32 m0, s10, 0x2000
	s_add_u32 s10, s36, 0x80080
	v_lshl_add_u64 v[202:203], v[216:217], 0, s[60:61]
	s_addc_u32 s11, s37, 0
	s_add_i32 s12, s13, s58
	global_load_lds_dwordx4 v[202:203], off
	v_lshl_add_u64 v[202:203], s[10:11], 0, v[66:67]
	s_mov_b32 m0, s12
	s_nop 0
	global_load_lds_dwordx4 v[202:203], off
	v_lshl_add_u64 v[202:203], s[10:11], 0, v[136:137]
	s_add_i32 m0, s12, 0x2000
	s_nop 0
	global_load_lds_dwordx4 v[202:203], off
	v_lshl_add_u64 v[202:203], v[218:219], 0, s[60:61]
	s_mov_b32 m0, s67
	s_nop 0
	global_load_lds_dwordx4 v[202:203], off
	v_lshl_add_u64 v[202:203], v[220:221], 0, s[60:61]
	s_mov_b32 m0, s68
	s_nop 0
	global_load_lds_dwordx4 v[202:203], off
	s_waitcnt vmcnt(8)
	s_waitcnt lgkmcnt(0)
	s_barrier
	s_setprio 1
	s_waitcnt lgkmcnt(0)
	v_mfma_f32_16x16x32_bf16 v[62:65], v[142:145], v[178:181], v[62:65]
	v_mfma_f32_16x16x32_bf16 v[58:61], v[154:157], v[178:181], v[58:61]
	v_mfma_f32_16x16x32_bf16 v[50:53], v[142:145], v[186:189], v[50:53]
	v_mfma_f32_16x16x32_bf16 v[42:45], v[154:157], v[186:189], v[42:45]
	v_mfma_f32_16x16x32_bf16 v[34:37], v[142:145], v[194:197], v[34:37]
	v_mfma_f32_16x16x32_bf16 v[26:29], v[154:157], v[194:197], v[26:29]
	v_mfma_f32_16x16x32_bf16 v[18:21], v[142:145], v[208:211], v[18:21]
	v_mfma_f32_16x16x32_bf16 v[10:13], v[154:157], v[208:211], v[10:13]
	v_mfma_f32_16x16x32_bf16 v[62:65], v[150:153], v[182:185], v[62:65]
	v_mfma_f32_16x16x32_bf16 v[58:61], v[158:161], v[182:185], v[58:61]
	v_mfma_f32_16x16x32_bf16 v[50:53], v[150:153], v[190:193], v[50:53]
	v_mfma_f32_16x16x32_bf16 v[42:45], v[158:161], v[190:193], v[42:45]
	v_mfma_f32_16x16x32_bf16 v[34:37], v[150:153], v[198:201], v[34:37]
	v_mfma_f32_16x16x32_bf16 v[26:29], v[158:161], v[198:201], v[26:29]
	v_mfma_f32_16x16x32_bf16 v[18:21], v[150:153], v[212:215], v[18:21]
	v_mfma_f32_16x16x32_bf16 v[10:13], v[158:161], v[212:215], v[10:13]
	s_setprio 0
	s_setprio 1
	v_mfma_f32_16x16x32_bf16 v[54:57], v[162:165], v[178:181], v[54:57]
	v_mfma_f32_16x16x32_bf16 v[46:49], v[170:173], v[178:181], v[46:49]
	v_mfma_f32_16x16x32_bf16 v[38:41], v[162:165], v[186:189], v[38:41]
	v_mfma_f32_16x16x32_bf16 v[30:33], v[170:173], v[186:189], v[30:33]
	v_mfma_f32_16x16x32_bf16 v[22:25], v[162:165], v[194:197], v[22:25]
	v_mfma_f32_16x16x32_bf16 v[14:17], v[170:173], v[194:197], v[14:17]
	v_mfma_f32_16x16x32_bf16 v[6:9], v[162:165], v[208:211], v[6:9]
	v_mfma_f32_16x16x32_bf16 v[2:5], v[170:173], v[208:211], v[2:5]
	v_mfma_f32_16x16x32_bf16 v[54:57], v[166:169], v[182:185], v[54:57]
	v_mfma_f32_16x16x32_bf16 v[46:49], v[174:177], v[182:185], v[46:49]
	v_mfma_f32_16x16x32_bf16 v[38:41], v[166:169], v[190:193], v[38:41]
	v_mfma_f32_16x16x32_bf16 v[30:33], v[174:177], v[190:193], v[30:33]
	v_mfma_f32_16x16x32_bf16 v[22:25], v[166:169], v[198:201], v[22:25]
	v_mfma_f32_16x16x32_bf16 v[14:17], v[174:177], v[198:201], v[14:17]
	v_mfma_f32_16x16x32_bf16 v[6:9], v[166:169], v[212:215], v[6:9]
	v_mfma_f32_16x16x32_bf16 v[2:5], v[174:177], v[212:215], v[2:5]
	s_setprio 0
	s_barrier
	s_add_i32 s71, s71, 2
	s_add_u32 s52, s52, 0x100
	s_addc_u32 s53, s53, 0
	s_add_u32 s8, s8, 0x100
	s_addc_u32 s9, s9, 0
	s_cmp_gt_u32 s71, 29

.LBB0_926:
	s_add_u32 s50, s50, 0x40080
	s_addc_u32 s51, s51, 0
	s_add_u32 s8, s36, 0x100
	v_mov_b32_e32 v2, 0
	s_addc_u32 s9, s37, 0
	s_mov_b32 s67, -2
	s_add_u32 s10, s50, 0xfffc0080
	s_addc_u32 s11, s51, -1
	s_add_i32 s12, 0, 0x10000
	s_cmp_eq_u32 s67, 12
	s_cselect_b32 s53, s45, s11
	s_cselect_b32 s52, s44, s10
	s_cselect_b32 s37, s47, s9
	s_cselect_b32 s36, s46, s8
	s_add_i32 s13, 0, 0x14000
	v_add_u32_e32 v144, s12, v171
	v_add_u32_e32 v174, s13, v171
	ds_read_b128 v[132:135], v144
	ds_read_b128 v[136:139], v144 offset:1024
	ds_read_b128 v[140:143], v144 offset:2048
	ds_read_b128 v[144:147], v144 offset:3072
	ds_read_b128 v[148:151], v174
	ds_read_b128 v[162:165], v174 offset:1024
	ds_read_b128 v[166:169], v174 offset:2048
	ds_read_b128 v[174:177], v174 offset:3072
	v_lshl_add_u64 v[202:203], s[50:51], 0, v[158:159]
	s_add_i32 m0, s55, 0xc000
	ds_read_b128 v[178:181], v173
	ds_read_b128 v[182:185], v173 offset:1024
	ds_read_b128 v[186:189], v173 offset:2048
	ds_read_b128 v[190:193], v173 offset:3072
	ds_read_b128 v[194:197], v173 offset:4096
	ds_read_b128 v[198:201], v173 offset:5120
	ds_read_b128 v[208:211], v173 offset:6144
	ds_read_b128 v[212:215], v173 offset:7168
	global_load_lds_dwordx4 v[202:203], off
	v_lshl_add_u64 v[202:203], s[50:51], 0, v[160:161]
	s_add_i32 m0, s55, 0xe000
	s_nop 0
	global_load_lds_dwordx4 v[202:203], off
	s_waitcnt vmcnt(8)
	s_waitcnt lgkmcnt(0)
	s_barrier
	s_setprio 1
	s_waitcnt lgkmcnt(0)
	v_mfma_f32_16x16x32_bf16 v[128:131], v[132:135], v[178:181], 0
	v_mfma_f32_16x16x32_bf16 v[124:127], v[140:143], v[178:181], 0
	v_mfma_f32_16x16x32_bf16 v[112:115], v[132:135], v[186:189], 0
	v_mfma_f32_16x16x32_bf16 v[108:111], v[140:143], v[186:189], 0
	v_mfma_f32_16x16x32_bf16 v[96:99], v[132:135], v[194:197], 0
	v_mfma_f32_16x16x32_bf16 v[92:95], v[140:143], v[194:197], 0
	v_mfma_f32_16x16x32_bf16 v[80:83], v[132:135], v[208:211], 0
	v_mfma_f32_16x16x32_bf16 v[76:79], v[140:143], v[208:211], 0
	v_mfma_f32_16x16x32_bf16 v[128:131], v[136:139], v[182:185], v[128:131]
	v_mfma_f32_16x16x32_bf16 v[124:127], v[144:147], v[182:185], v[124:127]
	v_mfma_f32_16x16x32_bf16 v[112:115], v[136:139], v[190:193], v[112:115]
	v_mfma_f32_16x16x32_bf16 v[108:111], v[144:147], v[190:193], v[108:111]
	v_mfma_f32_16x16x32_bf16 v[96:99], v[136:139], v[198:201], v[96:99]
	v_mfma_f32_16x16x32_bf16 v[92:95], v[144:147], v[198:201], v[92:95]
	v_mfma_f32_16x16x32_bf16 v[80:83], v[136:139], v[212:215], v[80:83]
	v_mfma_f32_16x16x32_bf16 v[76:79], v[144:147], v[212:215], v[76:79]
	s_setprio 0
	s_setprio 1
	v_mfma_f32_16x16x32_bf16 v[120:123], v[148:151], v[178:181], 0
	v_mfma_f32_16x16x32_bf16 v[116:119], v[166:169], v[178:181], 0
	v_mfma_f32_16x16x32_bf16 v[104:107], v[148:151], v[186:189], 0
	v_mfma_f32_16x16x32_bf16 v[100:103], v[166:169], v[186:189], 0
	v_mfma_f32_16x16x32_bf16 v[88:91], v[148:151], v[194:197], 0
	v_mfma_f32_16x16x32_bf16 v[84:87], v[166:169], v[194:197], 0
	v_mfma_f32_16x16x32_bf16 v[72:75], v[148:151], v[208:211], 0
	v_mfma_f32_16x16x32_bf16 v[68:71], v[166:169], v[208:211], 0
	v_mfma_f32_16x16x32_bf16 v[120:123], v[162:165], v[182:185], v[120:123]
	v_mfma_f32_16x16x32_bf16 v[116:119], v[174:177], v[182:185], v[116:119]
	v_mfma_f32_16x16x32_bf16 v[104:107], v[162:165], v[190:193], v[104:107]
	v_mfma_f32_16x16x32_bf16 v[100:103], v[174:177], v[190:193], v[100:103]
	v_mfma_f32_16x16x32_bf16 v[88:91], v[162:165], v[198:201], v[88:91]
	v_mfma_f32_16x16x32_bf16 v[84:87], v[174:177], v[198:201], v[84:87]
	v_mfma_f32_16x16x32_bf16 v[72:75], v[162:165], v[212:215], v[72:75]
	v_mfma_f32_16x16x32_bf16 v[68:71], v[174:177], v[212:215], v[68:71]
	s_setprio 0
	s_barrier
	s_add_i32 s10, s12, s54
	v_lshl_add_u64 v[202:203], s[36:37], 0, v[66:67]
	s_mov_b32 m0, s10
	ds_read_b128 v[178:181], v173 offset:16384
	ds_read_b128 v[182:185], v173 offset:17408
	ds_read_b128 v[186:189], v173 offset:18432
	ds_read_b128 v[190:193], v173 offset:19456
	ds_read_b128 v[194:197], v173 offset:20480
	ds_read_b128 v[198:201], v173 offset:21504
	ds_read_b128 v[208:211], v173 offset:22528
	ds_read_b128 v[212:215], v173 offset:23552
	global_load_lds_dwordx4 v[202:203], off
	s_add_i32 m0, s10, 0x2000
	s_add_u32 s10, s36, 0x40000
	v_lshl_add_u64 v[216:217], s[36:37], 0, v[156:157]
	s_addc_u32 s11, s37, 0
	s_add_i32 s12, s13, s54
	global_load_lds_dwordx4 v[216:217], off
	v_lshl_add_u64 v[218:219], s[10:11], 0, v[66:67]
	s_mov_b32 m0, s12
	v_lshl_add_u64 v[220:221], s[52:53], 0, v[154:155]
	global_load_lds_dwordx4 v[218:219], off
	v_lshl_add_u64 v[218:219], s[10:11], 0, v[156:157]
	s_add_i32 m0, s12, 0x2000
	s_nop 0
	global_load_lds_dwordx4 v[218:219], off
	v_lshl_add_u64 v[218:219], s[52:53], 0, v[152:153]
	s_mov_b32 m0, s55
	s_nop 0
	global_load_lds_dwordx4 v[218:219], off
	s_mov_b32 m0, s56
	s_nop 0
	global_load_lds_dwordx4 v[220:221], off
	s_waitcnt vmcnt(8)
	s_waitcnt lgkmcnt(0)
	s_barrier
	s_setprio 1
	s_waitcnt lgkmcnt(0)
	v_mfma_f32_16x16x32_bf16 v[62:65], v[132:135], v[178:181], 0
	v_mfma_f32_16x16x32_bf16 v[58:61], v[140:143], v[178:181], 0
	v_mfma_f32_16x16x32_bf16 v[46:49], v[132:135], v[186:189], 0
	v_mfma_f32_16x16x32_bf16 v[42:45], v[140:143], v[186:189], 0
	v_mfma_f32_16x16x32_bf16 v[30:33], v[132:135], v[194:197], 0
	v_mfma_f32_16x16x32_bf16 v[26:29], v[140:143], v[194:197], 0
	v_mfma_f32_16x16x32_bf16 v[14:17], v[132:135], v[208:211], 0
	v_mfma_f32_16x16x32_bf16 v[10:13], v[140:143], v[208:211], 0
	v_mfma_f32_16x16x32_bf16 v[62:65], v[136:139], v[182:185], v[62:65]
	v_mfma_f32_16x16x32_bf16 v[58:61], v[144:147], v[182:185], v[58:61]
	v_mfma_f32_16x16x32_bf16 v[46:49], v[136:139], v[190:193], v[46:49]
	v_mfma_f32_16x16x32_bf16 v[42:45], v[144:147], v[190:193], v[42:45]
	v_mfma_f32_16x16x32_bf16 v[30:33], v[136:139], v[198:201], v[30:33]
	v_mfma_f32_16x16x32_bf16 v[26:29], v[144:147], v[198:201], v[26:29]
	v_mfma_f32_16x16x32_bf16 v[14:17], v[136:139], v[212:215], v[14:17]
	v_mfma_f32_16x16x32_bf16 v[10:13], v[144:147], v[212:215], v[10:13]
	s_setprio 0
	s_setprio 1
	v_mfma_f32_16x16x32_bf16 v[54:57], v[148:151], v[178:181], 0
	v_mfma_f32_16x16x32_bf16 v[50:53], v[166:169], v[178:181], 0
	v_mfma_f32_16x16x32_bf16 v[38:41], v[148:151], v[186:189], 0
	v_mfma_f32_16x16x32_bf16 v[34:37], v[166:169], v[186:189], 0
	v_mfma_f32_16x16x32_bf16 v[22:25], v[148:151], v[194:197], 0
	v_mfma_f32_16x16x32_bf16 v[18:21], v[166:169], v[194:197], 0
	v_mfma_f32_16x16x32_bf16 v[6:9], v[148:151], v[208:211], 0
	v_mfma_f32_16x16x32_bf16 v[2:5], v[166:169], v[208:211], 0
	v_mfma_f32_16x16x32_bf16 v[54:57], v[162:165], v[182:185], v[54:57]
	v_mfma_f32_16x16x32_bf16 v[50:53], v[174:177], v[182:185], v[50:53]
	v_mfma_f32_16x16x32_bf16 v[38:41], v[162:165], v[190:193], v[38:41]
	v_mfma_f32_16x16x32_bf16 v[34:37], v[174:177], v[190:193], v[34:37]
	v_mfma_f32_16x16x32_bf16 v[22:25], v[162:165], v[198:201], v[22:25]
	v_mfma_f32_16x16x32_bf16 v[18:21], v[174:177], v[198:201], v[18:21]
	v_mfma_f32_16x16x32_bf16 v[6:9], v[162:165], v[212:215], v[6:9]
	v_mfma_f32_16x16x32_bf16 v[2:5], v[174:177], v[212:215], v[2:5]
	s_setprio 0
	s_barrier
	s_add_i32 s12, 0, 0x18000
	s_add_i32 s13, 0, 0x1c000
	v_add_u32_e32 v144, s12, v171
	v_add_u32_e32 v174, s13, v171
	ds_read_b128 v[132:135], v144
	ds_read_b128 v[136:139], v144 offset:1024
	ds_read_b128 v[140:143], v144 offset:2048
	ds_read_b128 v[144:147], v144 offset:3072
	ds_read_b128 v[148:151], v174
	ds_read_b128 v[162:165], v174 offset:1024
	ds_read_b128 v[166:169], v174 offset:2048
	ds_read_b128 v[174:177], v174 offset:3072
	s_add_u32 s10, s52, 0x40000
	s_addc_u32 s11, s53, 0
	s_mov_b32 m0, s57
	v_lshl_add_u64 v[222:223], s[10:11], 0, v[152:153]
	ds_read_b128 v[178:181], v173 offset:32768
	ds_read_b128 v[182:185], v173 offset:33792
	ds_read_b128 v[186:189], v173 offset:34816
	ds_read_b128 v[190:193], v173 offset:35840
	ds_read_b128 v[194:197], v173 offset:36864
	ds_read_b128 v[198:201], v173 offset:37888
	ds_read_b128 v[208:211], v173 offset:38912
	ds_read_b128 v[212:215], v173 offset:39936
	global_load_lds_dwordx4 v[222:223], off
	v_lshl_add_u64 v[222:223], s[10:11], 0, v[154:155]
	s_mov_b32 m0, s58
	s_nop 0
	global_load_lds_dwordx4 v[222:223], off
	s_waitcnt vmcnt(8)
	s_waitcnt lgkmcnt(0)
	s_barrier
	s_setprio 1
	s_waitcnt lgkmcnt(0)
	v_mfma_f32_16x16x32_bf16 v[128:131], v[132:135], v[178:181], v[128:131]
	v_mfma_f32_16x16x32_bf16 v[124:127], v[140:143], v[178:181], v[124:127]
	v_mfma_f32_16x16x32_bf16 v[112:115], v[132:135], v[186:189], v[112:115]
	v_mfma_f32_16x16x32_bf16 v[108:111], v[140:143], v[186:189], v[108:111]
	v_mfma_f32_16x16x32_bf16 v[96:99], v[132:135], v[194:197], v[96:99]
	v_mfma_f32_16x16x32_bf16 v[92:95], v[140:143], v[194:197], v[92:95]
	v_mfma_f32_16x16x32_bf16 v[80:83], v[132:135], v[208:211], v[80:83]
	v_mfma_f32_16x16x32_bf16 v[76:79], v[140:143], v[208:211], v[76:79]
	v_mfma_f32_16x16x32_bf16 v[128:131], v[136:139], v[182:185], v[128:131]
	v_mfma_f32_16x16x32_bf16 v[124:127], v[144:147], v[182:185], v[124:127]
	v_mfma_f32_16x16x32_bf16 v[112:115], v[136:139], v[190:193], v[112:115]
	v_mfma_f32_16x16x32_bf16 v[108:111], v[144:147], v[190:193], v[108:111]
	v_mfma_f32_16x16x32_bf16 v[96:99], v[136:139], v[198:201], v[96:99]
	v_mfma_f32_16x16x32_bf16 v[92:95], v[144:147], v[198:201], v[92:95]
	v_mfma_f32_16x16x32_bf16 v[80:83], v[136:139], v[212:215], v[80:83]
	v_mfma_f32_16x16x32_bf16 v[76:79], v[144:147], v[212:215], v[76:79]
	s_setprio 0
	s_setprio 1
	v_mfma_f32_16x16x32_bf16 v[120:123], v[148:151], v[178:181], v[120:123]
	v_mfma_f32_16x16x32_bf16 v[116:119], v[166:169], v[178:181], v[116:119]
	v_mfma_f32_16x16x32_bf16 v[104:107], v[148:151], v[186:189], v[104:107]
	v_mfma_f32_16x16x32_bf16 v[100:103], v[166:169], v[186:189], v[100:103]
	v_mfma_f32_16x16x32_bf16 v[88:91], v[148:151], v[194:197], v[88:91]
	v_mfma_f32_16x16x32_bf16 v[84:87], v[166:169], v[194:197], v[84:87]
	v_mfma_f32_16x16x32_bf16 v[72:75], v[148:151], v[208:211], v[72:75]
	v_mfma_f32_16x16x32_bf16 v[68:71], v[166:169], v[208:211], v[68:71]
	v_mfma_f32_16x16x32_bf16 v[120:123], v[162:165], v[182:185], v[120:123]
	v_mfma_f32_16x16x32_bf16 v[116:119], v[174:177], v[182:185], v[116:119]
	v_mfma_f32_16x16x32_bf16 v[104:107], v[162:165], v[190:193], v[104:107]
	v_mfma_f32_16x16x32_bf16 v[100:103], v[174:177], v[190:193], v[100:103]
	v_mfma_f32_16x16x32_bf16 v[88:91], v[162:165], v[198:201], v[88:91]
	v_mfma_f32_16x16x32_bf16 v[84:87], v[174:177], v[198:201], v[84:87]
	v_mfma_f32_16x16x32_bf16 v[72:75], v[162:165], v[212:215], v[72:75]
	v_mfma_f32_16x16x32_bf16 v[68:71], v[174:177], v[212:215], v[68:71]
	s_setprio 0
	s_barrier
	s_add_i32 s10, s12, s54
	v_lshl_add_u64 v[202:203], v[202:203], 0, s[60:61]
	s_mov_b32 m0, s10
	ds_read_b128 v[178:181], v173 offset:49152
	ds_read_b128 v[182:185], v173 offset:50176
	ds_read_b128 v[186:189], v173 offset:51200
	ds_read_b128 v[190:193], v173 offset:52224
	ds_read_b128 v[194:197], v173 offset:53248
	ds_read_b128 v[198:201], v173 offset:54272
	ds_read_b128 v[208:211], v173 offset:55296
	ds_read_b128 v[212:215], v173 offset:56320
	global_load_lds_dwordx4 v[202:203], off
	s_add_i32 m0, s10, 0x2000
	s_add_u32 s10, s36, 0x40080
	v_lshl_add_u64 v[202:203], v[216:217], 0, s[60:61]
	s_addc_u32 s11, s37, 0
	s_add_i32 s12, s13, s54
	global_load_lds_dwordx4 v[202:203], off
	v_lshl_add_u64 v[202:203], s[10:11], 0, v[66:67]
	s_mov_b32 m0, s12
	s_nop 0
	global_load_lds_dwordx4 v[202:203], off
	v_lshl_add_u64 v[202:203], s[10:11], 0, v[156:157]
	s_add_i32 m0, s12, 0x2000
	s_nop 0
	global_load_lds_dwordx4 v[202:203], off
	v_lshl_add_u64 v[202:203], v[218:219], 0, s[60:61]
	s_mov_b32 m0, s59
	s_nop 0
	global_load_lds_dwordx4 v[202:203], off
	v_lshl_add_u64 v[202:203], v[220:221], 0, s[60:61]
	s_mov_b32 m0, s64
	s_nop 0
	global_load_lds_dwordx4 v[202:203], off
	s_waitcnt vmcnt(8)
	s_waitcnt lgkmcnt(0)
	s_barrier
	s_setprio 1
	s_waitcnt lgkmcnt(0)
	v_mfma_f32_16x16x32_bf16 v[62:65], v[132:135], v[178:181], v[62:65]
	v_mfma_f32_16x16x32_bf16 v[58:61], v[140:143], v[178:181], v[58:61]
	v_mfma_f32_16x16x32_bf16 v[46:49], v[132:135], v[186:189], v[46:49]
	v_mfma_f32_16x16x32_bf16 v[42:45], v[140:143], v[186:189], v[42:45]
	v_mfma_f32_16x16x32_bf16 v[30:33], v[132:135], v[194:197], v[30:33]
	v_mfma_f32_16x16x32_bf16 v[26:29], v[140:143], v[194:197], v[26:29]
	v_mfma_f32_16x16x32_bf16 v[14:17], v[132:135], v[208:211], v[14:17]
	v_mfma_f32_16x16x32_bf16 v[10:13], v[140:143], v[208:211], v[10:13]
	v_mfma_f32_16x16x32_bf16 v[62:65], v[136:139], v[182:185], v[62:65]
	v_mfma_f32_16x16x32_bf16 v[58:61], v[144:147], v[182:185], v[58:61]
	v_mfma_f32_16x16x32_bf16 v[46:49], v[136:139], v[190:193], v[46:49]
	v_mfma_f32_16x16x32_bf16 v[42:45], v[144:147], v[190:193], v[42:45]
	v_mfma_f32_16x16x32_bf16 v[30:33], v[136:139], v[198:201], v[30:33]
	v_mfma_f32_16x16x32_bf16 v[26:29], v[144:147], v[198:201], v[26:29]
	v_mfma_f32_16x16x32_bf16 v[14:17], v[136:139], v[212:215], v[14:17]
	v_mfma_f32_16x16x32_bf16 v[10:13], v[144:147], v[212:215], v[10:13]
	s_setprio 0
	s_setprio 1
	v_mfma_f32_16x16x32_bf16 v[54:57], v[148:151], v[178:181], v[54:57]
	v_mfma_f32_16x16x32_bf16 v[50:53], v[166:169], v[178:181], v[50:53]
	v_mfma_f32_16x16x32_bf16 v[38:41], v[148:151], v[186:189], v[38:41]
	v_mfma_f32_16x16x32_bf16 v[34:37], v[166:169], v[186:189], v[34:37]
	v_mfma_f32_16x16x32_bf16 v[22:25], v[148:151], v[194:197], v[22:25]
	v_mfma_f32_16x16x32_bf16 v[18:21], v[166:169], v[194:197], v[18:21]
	v_mfma_f32_16x16x32_bf16 v[6:9], v[148:151], v[208:211], v[6:9]
	v_mfma_f32_16x16x32_bf16 v[2:5], v[166:169], v[208:211], v[2:5]
	v_mfma_f32_16x16x32_bf16 v[54:57], v[162:165], v[182:185], v[54:57]
	v_mfma_f32_16x16x32_bf16 v[50:53], v[174:177], v[182:185], v[50:53]
	v_mfma_f32_16x16x32_bf16 v[38:41], v[162:165], v[190:193], v[38:41]
	v_mfma_f32_16x16x32_bf16 v[34:37], v[174:177], v[190:193], v[34:37]
	v_mfma_f32_16x16x32_bf16 v[22:25], v[162:165], v[198:201], v[22:25]
	v_mfma_f32_16x16x32_bf16 v[18:21], v[174:177], v[198:201], v[18:21]
	v_mfma_f32_16x16x32_bf16 v[6:9], v[162:165], v[212:215], v[6:9]
	v_mfma_f32_16x16x32_bf16 v[2:5], v[174:177], v[212:215], v[2:5]
	s_setprio 0
	s_barrier
	s_add_i32 s67, s67, 2
	s_add_u32 s50, s50, 0x100
	s_addc_u32 s51, s51, 0
	s_add_u32 s8, s8, 0x100
	s_addc_u32 s9, s9, 0
	s_cmp_gt_u32 s67, 13

.LBB0_997:
	s_add_u32 s34, s34, 0x40080
	s_addc_u32 s35, s35, 0
	s_add_u32 s8, s36, 0x100
	v_mov_b32_e32 v2, 0
	s_addc_u32 s9, s37, 0
	s_mov_b32 s26, -2
	s_add_u32 s10, s34, 0xfffc0080
	s_addc_u32 s11, s35, -1
	s_add_i32 s42, 0, 0x10000
	s_cmp_eq_u32 s26, 12
	s_cselect_b32 s41, s55, s11
	s_cselect_b32 s40, s54, s10
	s_cselect_b32 s37, s57, s9
	s_cselect_b32 s36, s56, s8
	s_add_i32 s12, 0, 0x14000
	v_add_u32_e32 v72, s42, v218
	v_add_u32_e32 v96, s12, v218
	ds_read_b128 v[58:61], v72
	ds_read_b128 v[62:65], v72 offset:1024
	ds_read_b128 v[68:71], v72 offset:2048
	ds_read_b128 v[72:75], v72 offset:3072
	ds_read_b128 v[84:87], v96
	ds_read_b128 v[88:91], v96 offset:1024
	ds_read_b128 v[92:95], v96 offset:2048
	ds_read_b128 v[96:99], v96 offset:3072
	v_lshl_add_u64 v[202:203], s[34:35], 0, v[186:187]
	s_add_i32 m0, s85, 0xc000
	ds_read_b128 v[164:167], v219
	ds_read_b128 v[168:171], v219 offset:1024
	ds_read_b128 v[190:193], v219 offset:2048
	ds_read_b128 v[194:197], v219 offset:3072
	ds_read_b128 v[198:201], v219 offset:4096
	ds_read_b128 v[208:211], v219 offset:5120
	ds_read_b128 v[212:215], v219 offset:6144
	ds_read_b128 v[220:223], v219 offset:7168
	global_load_lds_dwordx4 v[202:203], off
	v_lshl_add_u64 v[202:203], s[34:35], 0, v[188:189]
	s_add_i32 m0, s85, 0xe000
	s_nop 0
	global_load_lds_dwordx4 v[202:203], off
	s_waitcnt vmcnt(8)
	s_waitcnt lgkmcnt(0)
	s_barrier
	s_setprio 1
	s_waitcnt lgkmcnt(0)
	v_mfma_f32_16x16x32_bf16 v[160:163], v[58:61], v[164:167], 0
	v_mfma_f32_16x16x32_bf16 v[156:159], v[68:71], v[164:167], 0
	v_mfma_f32_16x16x32_bf16 v[144:147], v[58:61], v[190:193], 0
	v_mfma_f32_16x16x32_bf16 v[140:143], v[68:71], v[190:193], 0
	v_mfma_f32_16x16x32_bf16 v[128:131], v[58:61], v[198:201], 0
	v_mfma_f32_16x16x32_bf16 v[124:127], v[68:71], v[198:201], 0
	v_mfma_f32_16x16x32_bf16 v[112:115], v[58:61], v[212:215], 0
	v_mfma_f32_16x16x32_bf16 v[108:111], v[68:71], v[212:215], 0
	v_mfma_f32_16x16x32_bf16 v[160:163], v[62:65], v[168:171], v[160:163]
	v_mfma_f32_16x16x32_bf16 v[156:159], v[72:75], v[168:171], v[156:159]
	v_mfma_f32_16x16x32_bf16 v[144:147], v[62:65], v[194:197], v[144:147]
	v_mfma_f32_16x16x32_bf16 v[140:143], v[72:75], v[194:197], v[140:143]
	v_mfma_f32_16x16x32_bf16 v[128:131], v[62:65], v[208:211], v[128:131]
	v_mfma_f32_16x16x32_bf16 v[124:127], v[72:75], v[208:211], v[124:127]
	v_mfma_f32_16x16x32_bf16 v[112:115], v[62:65], v[220:223], v[112:115]
	v_mfma_f32_16x16x32_bf16 v[108:111], v[72:75], v[220:223], v[108:111]
	s_setprio 0
	s_setprio 1
	v_mfma_f32_16x16x32_bf16 v[152:155], v[84:87], v[164:167], 0
	v_mfma_f32_16x16x32_bf16 v[148:151], v[92:95], v[164:167], 0
	v_mfma_f32_16x16x32_bf16 v[136:139], v[84:87], v[190:193], 0
	v_mfma_f32_16x16x32_bf16 v[132:135], v[92:95], v[190:193], 0
	v_mfma_f32_16x16x32_bf16 v[120:123], v[84:87], v[198:201], 0
	v_mfma_f32_16x16x32_bf16 v[116:119], v[92:95], v[198:201], 0
	v_mfma_f32_16x16x32_bf16 v[104:107], v[84:87], v[212:215], 0
	v_mfma_f32_16x16x32_bf16 v[100:103], v[92:95], v[212:215], 0
	v_mfma_f32_16x16x32_bf16 v[152:155], v[88:91], v[168:171], v[152:155]
	v_mfma_f32_16x16x32_bf16 v[148:151], v[96:99], v[168:171], v[148:151]
	v_mfma_f32_16x16x32_bf16 v[136:139], v[88:91], v[194:197], v[136:139]
	v_mfma_f32_16x16x32_bf16 v[132:135], v[96:99], v[194:197], v[132:135]
	v_mfma_f32_16x16x32_bf16 v[120:123], v[88:91], v[208:211], v[120:123]
	v_mfma_f32_16x16x32_bf16 v[116:119], v[96:99], v[208:211], v[116:119]
	v_mfma_f32_16x16x32_bf16 v[104:107], v[88:91], v[220:223], v[104:107]
	v_mfma_f32_16x16x32_bf16 v[100:103], v[96:99], v[220:223], v[100:103]
	s_setprio 0
	s_barrier
	s_add_i32 s10, s42, s84
	v_lshl_add_u64 v[202:203], s[36:37], 0, v[174:175]
	s_mov_b32 m0, s10
	ds_read_b128 v[164:167], v219 offset:16384
	ds_read_b128 v[168:171], v219 offset:17408
	ds_read_b128 v[190:193], v219 offset:18432
	ds_read_b128 v[194:197], v219 offset:19456
	ds_read_b128 v[198:201], v219 offset:20480
	ds_read_b128 v[208:211], v219 offset:21504
	ds_read_b128 v[212:215], v219 offset:22528
	ds_read_b128 v[220:223], v219 offset:23552
	global_load_lds_dwordx4 v[202:203], off
	s_add_i32 m0, s10, 0x2000
	s_add_u32 s10, s36, 0x40000
	v_lshl_add_u64 v[224:225], s[36:37], 0, v[178:179]
	s_addc_u32 s11, s37, 0
	s_add_i32 s12, s12, s84
	global_load_lds_dwordx4 v[224:225], off
	v_lshl_add_u64 v[226:227], s[10:11], 0, v[174:175]
	s_mov_b32 m0, s12
	v_lshl_add_u64 v[228:229], s[40:41], 0, v[176:177]
	global_load_lds_dwordx4 v[226:227], off
	v_lshl_add_u64 v[226:227], s[10:11], 0, v[178:179]
	s_add_i32 m0, s12, 0x2000
	s_nop 0
	global_load_lds_dwordx4 v[226:227], off
	v_lshl_add_u64 v[226:227], s[40:41], 0, v[172:173]
	s_mov_b32 m0, s85
	s_nop 0
	global_load_lds_dwordx4 v[226:227], off
	s_mov_b32 m0, s86
	s_nop 0
	global_load_lds_dwordx4 v[228:229], off
	s_waitcnt vmcnt(8)
	s_waitcnt lgkmcnt(0)
	s_barrier
	s_setprio 1
	s_waitcnt lgkmcnt(0)
	v_mfma_f32_16x16x32_bf16 v[80:83], v[58:61], v[164:167], 0
	v_mfma_f32_16x16x32_bf16 v[76:79], v[68:71], v[164:167], 0
	v_mfma_f32_16x16x32_bf16 v[46:49], v[58:61], v[190:193], 0
	v_mfma_f32_16x16x32_bf16 v[42:45], v[68:71], v[190:193], 0
	v_mfma_f32_16x16x32_bf16 v[30:33], v[58:61], v[198:201], 0
	v_mfma_f32_16x16x32_bf16 v[26:29], v[68:71], v[198:201], 0
	v_mfma_f32_16x16x32_bf16 v[14:17], v[58:61], v[212:215], 0
	v_mfma_f32_16x16x32_bf16 v[10:13], v[68:71], v[212:215], 0
	v_mfma_f32_16x16x32_bf16 v[80:83], v[62:65], v[168:171], v[80:83]
	v_mfma_f32_16x16x32_bf16 v[76:79], v[72:75], v[168:171], v[76:79]
	v_mfma_f32_16x16x32_bf16 v[46:49], v[62:65], v[194:197], v[46:49]
	v_mfma_f32_16x16x32_bf16 v[42:45], v[72:75], v[194:197], v[42:45]
	v_mfma_f32_16x16x32_bf16 v[30:33], v[62:65], v[208:211], v[30:33]
	v_mfma_f32_16x16x32_bf16 v[26:29], v[72:75], v[208:211], v[26:29]
	v_mfma_f32_16x16x32_bf16 v[14:17], v[62:65], v[220:223], v[14:17]
	v_mfma_f32_16x16x32_bf16 v[10:13], v[72:75], v[220:223], v[10:13]
	s_setprio 0
	s_setprio 1
	v_mfma_f32_16x16x32_bf16 v[54:57], v[84:87], v[164:167], 0
	v_mfma_f32_16x16x32_bf16 v[50:53], v[92:95], v[164:167], 0
	v_mfma_f32_16x16x32_bf16 v[38:41], v[84:87], v[190:193], 0
	v_mfma_f32_16x16x32_bf16 v[34:37], v[92:95], v[190:193], 0
	v_mfma_f32_16x16x32_bf16 v[22:25], v[84:87], v[198:201], 0
	v_mfma_f32_16x16x32_bf16 v[18:21], v[92:95], v[198:201], 0
	v_mfma_f32_16x16x32_bf16 v[6:9], v[84:87], v[212:215], 0
	v_mfma_f32_16x16x32_bf16 v[2:5], v[92:95], v[212:215], 0
	v_mfma_f32_16x16x32_bf16 v[54:57], v[88:91], v[168:171], v[54:57]
	v_mfma_f32_16x16x32_bf16 v[50:53], v[96:99], v[168:171], v[50:53]
	v_mfma_f32_16x16x32_bf16 v[38:41], v[88:91], v[194:197], v[38:41]
	v_mfma_f32_16x16x32_bf16 v[34:37], v[96:99], v[194:197], v[34:37]
	v_mfma_f32_16x16x32_bf16 v[22:25], v[88:91], v[208:211], v[22:25]
	v_mfma_f32_16x16x32_bf16 v[18:21], v[96:99], v[208:211], v[18:21]
	v_mfma_f32_16x16x32_bf16 v[6:9], v[88:91], v[220:223], v[6:9]
	v_mfma_f32_16x16x32_bf16 v[2:5], v[96:99], v[220:223], v[2:5]
	s_setprio 0
	s_barrier
	s_add_i32 s43, 0, 0x18000
	s_add_i32 s12, 0, 0x1c000
	v_add_u32_e32 v72, s43, v218
	v_add_u32_e32 v96, s12, v218
	ds_read_b128 v[58:61], v72
	ds_read_b128 v[62:65], v72 offset:1024
	ds_read_b128 v[68:71], v72 offset:2048
	ds_read_b128 v[72:75], v72 offset:3072
	ds_read_b128 v[84:87], v96
	ds_read_b128 v[88:91], v96 offset:1024
	ds_read_b128 v[92:95], v96 offset:2048
	ds_read_b128 v[96:99], v96 offset:3072
	s_add_u32 s10, s40, 0x40000
	s_addc_u32 s11, s41, 0
	s_mov_b32 m0, s87
	v_lshl_add_u64 v[230:231], s[10:11], 0, v[172:173]
	ds_read_b128 v[164:167], v219 offset:32768
	ds_read_b128 v[168:171], v219 offset:33792
	ds_read_b128 v[190:193], v219 offset:34816
	ds_read_b128 v[194:197], v219 offset:35840
	ds_read_b128 v[198:201], v219 offset:36864
	ds_read_b128 v[208:211], v219 offset:37888
	ds_read_b128 v[212:215], v219 offset:38912
	ds_read_b128 v[220:223], v219 offset:39936
	global_load_lds_dwordx4 v[230:231], off
	v_lshl_add_u64 v[230:231], s[10:11], 0, v[176:177]
	s_mov_b32 m0, s88
	s_nop 0
	global_load_lds_dwordx4 v[230:231], off
	s_waitcnt vmcnt(8)
	s_waitcnt lgkmcnt(0)
	s_barrier
	s_setprio 1
	s_waitcnt lgkmcnt(0)
	v_mfma_f32_16x16x32_bf16 v[160:163], v[58:61], v[164:167], v[160:163]
	v_mfma_f32_16x16x32_bf16 v[156:159], v[68:71], v[164:167], v[156:159]
	v_mfma_f32_16x16x32_bf16 v[144:147], v[58:61], v[190:193], v[144:147]
	v_mfma_f32_16x16x32_bf16 v[140:143], v[68:71], v[190:193], v[140:143]
	v_mfma_f32_16x16x32_bf16 v[128:131], v[58:61], v[198:201], v[128:131]
	v_mfma_f32_16x16x32_bf16 v[124:127], v[68:71], v[198:201], v[124:127]
	v_mfma_f32_16x16x32_bf16 v[112:115], v[58:61], v[212:215], v[112:115]
	v_mfma_f32_16x16x32_bf16 v[108:111], v[68:71], v[212:215], v[108:111]
	v_mfma_f32_16x16x32_bf16 v[160:163], v[62:65], v[168:171], v[160:163]
	v_mfma_f32_16x16x32_bf16 v[156:159], v[72:75], v[168:171], v[156:159]
	v_mfma_f32_16x16x32_bf16 v[144:147], v[62:65], v[194:197], v[144:147]
	v_mfma_f32_16x16x32_bf16 v[140:143], v[72:75], v[194:197], v[140:143]
	v_mfma_f32_16x16x32_bf16 v[128:131], v[62:65], v[208:211], v[128:131]
	v_mfma_f32_16x16x32_bf16 v[124:127], v[72:75], v[208:211], v[124:127]
	v_mfma_f32_16x16x32_bf16 v[112:115], v[62:65], v[220:223], v[112:115]
	v_mfma_f32_16x16x32_bf16 v[108:111], v[72:75], v[220:223], v[108:111]
	s_setprio 0
	s_setprio 1
	v_mfma_f32_16x16x32_bf16 v[152:155], v[84:87], v[164:167], v[152:155]
	v_mfma_f32_16x16x32_bf16 v[148:151], v[92:95], v[164:167], v[148:151]
	v_mfma_f32_16x16x32_bf16 v[136:139], v[84:87], v[190:193], v[136:139]
	v_mfma_f32_16x16x32_bf16 v[132:135], v[92:95], v[190:193], v[132:135]
	v_mfma_f32_16x16x32_bf16 v[120:123], v[84:87], v[198:201], v[120:123]
	v_mfma_f32_16x16x32_bf16 v[116:119], v[92:95], v[198:201], v[116:119]
	v_mfma_f32_16x16x32_bf16 v[104:107], v[84:87], v[212:215], v[104:107]
	v_mfma_f32_16x16x32_bf16 v[100:103], v[92:95], v[212:215], v[100:103]
	v_mfma_f32_16x16x32_bf16 v[152:155], v[88:91], v[168:171], v[152:155]
	v_mfma_f32_16x16x32_bf16 v[148:151], v[96:99], v[168:171], v[148:151]
	v_mfma_f32_16x16x32_bf16 v[136:139], v[88:91], v[194:197], v[136:139]
	v_mfma_f32_16x16x32_bf16 v[132:135], v[96:99], v[194:197], v[132:135]
	v_mfma_f32_16x16x32_bf16 v[120:123], v[88:91], v[208:211], v[120:123]
	v_mfma_f32_16x16x32_bf16 v[116:119], v[96:99], v[208:211], v[116:119]
	v_mfma_f32_16x16x32_bf16 v[104:107], v[88:91], v[220:223], v[104:107]
	v_mfma_f32_16x16x32_bf16 v[100:103], v[96:99], v[220:223], v[100:103]
	s_setprio 0
	s_barrier
	s_add_i32 s10, s43, s84
	v_lshl_add_u64 v[202:203], v[202:203], 0, s[60:61]
	s_mov_b32 m0, s10
	ds_read_b128 v[164:167], v219 offset:49152
	ds_read_b128 v[168:171], v219 offset:50176
	ds_read_b128 v[190:193], v219 offset:51200
	ds_read_b128 v[194:197], v219 offset:52224
	ds_read_b128 v[198:201], v219 offset:53248
	ds_read_b128 v[208:211], v219 offset:54272
	ds_read_b128 v[212:215], v219 offset:55296
	ds_read_b128 v[220:223], v219 offset:56320
	global_load_lds_dwordx4 v[202:203], off
	s_add_i32 m0, s10, 0x2000
	s_add_u32 s10, s36, 0x40080
	v_lshl_add_u64 v[202:203], v[224:225], 0, s[60:61]
	s_addc_u32 s11, s37, 0
	s_add_i32 s12, s12, s84
	global_load_lds_dwordx4 v[202:203], off
	v_lshl_add_u64 v[202:203], s[10:11], 0, v[174:175]
	s_mov_b32 m0, s12
	s_nop 0
	global_load_lds_dwordx4 v[202:203], off
	v_lshl_add_u64 v[202:203], s[10:11], 0, v[178:179]
	s_add_i32 m0, s12, 0x2000
	s_nop 0
	global_load_lds_dwordx4 v[202:203], off
	v_lshl_add_u64 v[202:203], v[226:227], 0, s[60:61]
	s_mov_b32 m0, s72
	s_nop 0
	global_load_lds_dwordx4 v[202:203], off
	v_lshl_add_u64 v[202:203], v[228:229], 0, s[60:61]
	s_mov_b32 m0, s90
	s_nop 0
	global_load_lds_dwordx4 v[202:203], off
	s_waitcnt vmcnt(8)
	s_waitcnt lgkmcnt(0)
	s_barrier
	s_setprio 1
	s_waitcnt lgkmcnt(0)
	v_mfma_f32_16x16x32_bf16 v[80:83], v[58:61], v[164:167], v[80:83]
	v_mfma_f32_16x16x32_bf16 v[76:79], v[68:71], v[164:167], v[76:79]
	v_mfma_f32_16x16x32_bf16 v[46:49], v[58:61], v[190:193], v[46:49]
	v_mfma_f32_16x16x32_bf16 v[42:45], v[68:71], v[190:193], v[42:45]
	v_mfma_f32_16x16x32_bf16 v[30:33], v[58:61], v[198:201], v[30:33]
	v_mfma_f32_16x16x32_bf16 v[26:29], v[68:71], v[198:201], v[26:29]
	v_mfma_f32_16x16x32_bf16 v[14:17], v[58:61], v[212:215], v[14:17]
	v_mfma_f32_16x16x32_bf16 v[10:13], v[68:71], v[212:215], v[10:13]
	v_mfma_f32_16x16x32_bf16 v[80:83], v[62:65], v[168:171], v[80:83]
	v_mfma_f32_16x16x32_bf16 v[76:79], v[72:75], v[168:171], v[76:79]
	v_mfma_f32_16x16x32_bf16 v[46:49], v[62:65], v[194:197], v[46:49]
	v_mfma_f32_16x16x32_bf16 v[42:45], v[72:75], v[194:197], v[42:45]
	v_mfma_f32_16x16x32_bf16 v[30:33], v[62:65], v[208:211], v[30:33]
	v_mfma_f32_16x16x32_bf16 v[26:29], v[72:75], v[208:211], v[26:29]
	v_mfma_f32_16x16x32_bf16 v[14:17], v[62:65], v[220:223], v[14:17]
	v_mfma_f32_16x16x32_bf16 v[10:13], v[72:75], v[220:223], v[10:13]
	s_setprio 0
	s_setprio 1
	v_mfma_f32_16x16x32_bf16 v[54:57], v[84:87], v[164:167], v[54:57]
	v_mfma_f32_16x16x32_bf16 v[50:53], v[92:95], v[164:167], v[50:53]
	v_mfma_f32_16x16x32_bf16 v[38:41], v[84:87], v[190:193], v[38:41]
	v_mfma_f32_16x16x32_bf16 v[34:37], v[92:95], v[190:193], v[34:37]
	v_mfma_f32_16x16x32_bf16 v[22:25], v[84:87], v[198:201], v[22:25]
	v_mfma_f32_16x16x32_bf16 v[18:21], v[92:95], v[198:201], v[18:21]
	v_mfma_f32_16x16x32_bf16 v[6:9], v[84:87], v[212:215], v[6:9]
	v_mfma_f32_16x16x32_bf16 v[2:5], v[92:95], v[212:215], v[2:5]
	v_mfma_f32_16x16x32_bf16 v[54:57], v[88:91], v[168:171], v[54:57]
	v_mfma_f32_16x16x32_bf16 v[50:53], v[96:99], v[168:171], v[50:53]
	v_mfma_f32_16x16x32_bf16 v[38:41], v[88:91], v[194:197], v[38:41]
	v_mfma_f32_16x16x32_bf16 v[34:37], v[96:99], v[194:197], v[34:37]
	v_mfma_f32_16x16x32_bf16 v[22:25], v[88:91], v[208:211], v[22:25]
	v_mfma_f32_16x16x32_bf16 v[18:21], v[96:99], v[208:211], v[18:21]
	v_mfma_f32_16x16x32_bf16 v[6:9], v[88:91], v[220:223], v[6:9]
	v_mfma_f32_16x16x32_bf16 v[2:5], v[96:99], v[220:223], v[2:5]
	s_setprio 0
	s_barrier
	s_add_i32 s26, s26, 2
	s_add_u32 s34, s34, 0x100
	s_addc_u32 s35, s35, 0
	s_add_u32 s8, s8, 0x100
	s_addc_u32 s9, s9, 0
	s_cmp_gt_u32 s26, 13
